# v9: + P1 side job staged in VGPRs (two slots), K-loop vmcnt waits 8->11 in steady state (m1)
# speedup vs baseline: 1.0102x; 1.0061x over previous
.LBB0_163:
	s_add_i32 s69, s41, 0x18000
	s_mov_b64 s[24:25], 0x80
	s_lshl_b32 s2, s2, 12
	v_lshl_add_u64 v[10:11], v[10:11], 0, s[24:25]
	s_mov_b32 m0, s69
	s_add_i32 s70, s41, 0x1a000
	s_lshl_b32 s68, s96, 7
	s_lshl_b32 s7, s3, 13
	s_and_b32 s9, s2, 0x3000
	s_waitcnt vmcnt(2)
	s_barrier
	global_load_lds_dwordx4 v[10:11], off
	v_lshl_add_u64 v[8:9], v[8:9], 0, s[24:25]
	s_mov_b32 m0, s70
	s_add_i32 s71, s41, 0x8000
	s_add_i32 s72, s41, 0xa000
	global_load_lds_dwordx4 v[8:9], off
	v_lshl_add_u64 v[4:5], v[4:5], 0, s[24:25]
	s_mov_b32 m0, s71
	s_add_u32 s2, s4, 0x80080
	global_load_lds_dwordx4 v[4:5], off
	v_lshl_add_u64 v[4:5], v[6:7], 0, s[24:25]
	s_mov_b32 m0, s72
	s_addc_u32 s3, s5, 0
	s_add_i32 s73, s41, 0x1c000
	global_load_lds_dwordx4 v[4:5], off
	v_lshl_add_u64 v[4:5], s[2:3], 0, v[212:213]
	s_mov_b32 m0, s73
	s_add_i32 s75, s41, 0x1e000
	global_load_lds_dwordx4 v[4:5], off
	v_lshl_add_u64 v[4:5], s[2:3], 0, v[216:217]
	s_mov_b32 m0, s75
	v_and_b32_e32 v1, 48, v0
	global_load_lds_dwordx4 v[4:5], off
	v_lshlrev_b32_e32 v4, 6, v0
	v_and_b32_e32 v4, 0x3c0, v4
	v_and_b32_e32 v6, 32, v208
	v_or_b32_e32 v5, v4, v1
	v_bitop3_b32 v1, v4, v6, v1 bitop3:0x36
	v_lshlrev_b32_e32 v4, 9, v0
	v_bitop3_b32 v6, s7, v5, v6 bitop3:0xf6
	v_and_b32_e32 v4, 0x30000, v4
	v_lshlrev_b32_e32 v5, 12, v13
	v_or3_b32 v4, v2, v4, v5
	v_add_u32_e32 v218, v4, v12
	v_lshlrev_b32_e32 v4, 5, v15
	s_add_i32 s2, 0, 0x26000
	v_and_b32_e32 v4, 0x70000, v4
	v_or_b32_e32 v7, s9, v1
	s_waitcnt vmcnt(6)
	v_add_u32_e32 v1, s2, v14
	s_add_i32 s2, 0, 0x24000
	s_add_i32 s74, s68, -1
	v_or3_b32 v2, v2, v4, v5
	v_mov_b32_e32 v4, v3
	v_mov_b32_e32 v5, v3
	v_add_u32_e32 v234, 0, v6
	v_mbcnt_lo_u32_b32 v6, -1, 0
	s_cmpk_lt_u32 s8, 0x100
	v_add_u32_e32 v220, v2, v12
	v_mov_b32_e32 v2, v3
	v_add_u32_e32 v209, 0, v7
	v_mbcnt_hi_u32_b32 v235, -1, v6
	v_mov_b64_e32 v[8:9], v[4:5]
	v_mov_b64_e32 v[12:13], v[4:5]
	v_add_u32_e32 v207, s2, v14
	s_cselect_b64 s[38:39], -1, 0
	s_ashr_i32 s76, s96, 31
	v_mov_b32_e32 v219, v3
	v_mov_b32_e32 v221, v3
	s_mov_b64 s[2:3], 0
	v_mov_b64_e32 v[222:223], 0x300
	v_mov_b64_e32 v[224:225], 0x2ff
	v_add_u32_e32 v232, 0x10000, v209
	v_add_u32_e32 v233, 0x14000, v209
	s_mov_b32 s40, 0x42800000
	s_mov_b64 s[42:43], 0x4000
	s_movk_i32 s78, 0x3100
	v_mov_b32_e32 v236, 0x3e38aa3b
	v_mov_b64_e32 v[6:7], v[2:3]
	v_mov_b64_e32 v[10:11], v[2:3]
	s_mov_b32 s77, 0
	s_mov_b32 s98, -1
	s_mov_b32 s99, -1
	s_mov_b32 s100, 0
	s_mov_b32 s90, s91
	s_barrier

.LBB0_167:
	s_barrier
	s_setprio 1
	s_waitcnt lgkmcnt(0)
	v_mfma_f32_16x16x32_bf16 v[138:141], v[158:161], v[198:201], v[138:141]
	v_mfma_f32_16x16x32_bf16 v[134:137], v[166:169], v[198:201], v[134:137]
	v_mfma_f32_16x16x32_bf16 v[122:125], v[158:161], v[190:193], v[122:125]
	v_mfma_f32_16x16x32_bf16 v[118:121], v[166:169], v[190:193], v[118:121]
	v_mfma_f32_16x16x32_bf16 v[106:109], v[158:161], v[182:185], v[106:109]
	v_mfma_f32_16x16x32_bf16 v[102:105], v[166:169], v[182:185], v[102:105]
	v_mfma_f32_16x16x32_bf16 v[90:93], v[158:161], v[174:177], v[90:93]
	v_mfma_f32_16x16x32_bf16 v[86:89], v[166:169], v[174:177], v[86:89]
	v_mfma_f32_16x16x32_bf16 v[138:141], v[162:165], v[202:205], v[138:141]
	v_mfma_f32_16x16x32_bf16 v[134:137], v[170:173], v[202:205], v[134:137]
	v_mfma_f32_16x16x32_bf16 v[122:125], v[162:165], v[194:197], v[122:125]
	v_mfma_f32_16x16x32_bf16 v[118:121], v[170:173], v[194:197], v[118:121]
	v_mfma_f32_16x16x32_bf16 v[106:109], v[162:165], v[186:189], v[106:109]
	v_mfma_f32_16x16x32_bf16 v[102:105], v[170:173], v[186:189], v[102:105]
	v_mfma_f32_16x16x32_bf16 v[90:93], v[162:165], v[178:181], v[90:93]
	v_mfma_f32_16x16x32_bf16 v[86:89], v[170:173], v[178:181], v[86:89]
	s_setprio 0
	s_setprio 1
	v_mfma_f32_16x16x32_bf16 v[130:133], v[142:145], v[198:201], v[130:133]
	v_mfma_f32_16x16x32_bf16 v[126:129], v[150:153], v[198:201], v[126:129]
	v_mfma_f32_16x16x32_bf16 v[114:117], v[142:145], v[190:193], v[114:117]
	v_mfma_f32_16x16x32_bf16 v[110:113], v[150:153], v[190:193], v[110:113]
	v_mfma_f32_16x16x32_bf16 v[98:101], v[142:145], v[182:185], v[98:101]
	v_mfma_f32_16x16x32_bf16 v[94:97], v[150:153], v[182:185], v[94:97]
	v_mfma_f32_16x16x32_bf16 v[82:85], v[142:145], v[174:177], v[82:85]
	v_mfma_f32_16x16x32_bf16 v[78:81], v[150:153], v[174:177], v[78:81]
	v_mfma_f32_16x16x32_bf16 v[130:133], v[146:149], v[202:205], v[130:133]
	v_mfma_f32_16x16x32_bf16 v[126:129], v[154:157], v[202:205], v[126:129]
	v_mfma_f32_16x16x32_bf16 v[114:117], v[146:149], v[194:197], v[114:117]
	v_mfma_f32_16x16x32_bf16 v[110:113], v[154:157], v[194:197], v[110:113]
	v_mfma_f32_16x16x32_bf16 v[98:101], v[146:149], v[186:189], v[98:101]
	v_mfma_f32_16x16x32_bf16 v[94:97], v[154:157], v[186:189], v[94:97]
	v_mfma_f32_16x16x32_bf16 v[82:85], v[146:149], v[178:181], v[82:85]
	v_mfma_f32_16x16x32_bf16 v[78:81], v[154:157], v[178:181], v[78:81]
	s_setprio 0
	s_barrier
	s_mov_b32 m0, s69
	v_lshl_add_u64 v[4:5], v[4:5], 0, s[24:25]
	s_add_u32 s4, s56, 0x80080
	ds_read_b128 v[174:177], v234 offset:49152
	ds_read_b128 v[178:181], v234 offset:50176
	ds_read_b128 v[182:185], v234 offset:51200
	ds_read_b128 v[186:189], v234 offset:52224
	ds_read_b128 v[190:193], v234 offset:53248
	ds_read_b128 v[194:197], v234 offset:54272
	ds_read_b128 v[198:201], v234 offset:55296
	ds_read_b128 v[202:205], v234 offset:56320
	global_load_lds_dwordx4 v[4:5], off
	v_lshl_add_u64 v[4:5], v[226:227], 0, s[24:25]
	s_mov_b32 m0, s70
	s_addc_u32 s5, s57, 0
	global_load_lds_dwordx4 v[4:5], off
	v_lshl_add_u64 v[4:5], s[4:5], 0, v[212:213]
	s_mov_b32 m0, s73
	s_nop 0
	global_load_lds_dwordx4 v[4:5], off
	v_lshl_add_u64 v[4:5], s[4:5], 0, v[216:217]
	s_mov_b32 m0, s75
	s_nop 0
	global_load_lds_dwordx4 v[4:5], off
	v_lshl_add_u64 v[4:5], v[228:229], 0, s[24:25]
	s_mov_b32 m0, s71
	s_nop 0
	global_load_lds_dwordx4 v[4:5], off
	v_lshl_add_u64 v[4:5], v[230:231], 0, s[24:25]
	s_mov_b32 m0, s72
	s_nop 0
	global_load_lds_dwordx4 v[4:5], off
	s_cmp_eq_u32 s100, 3
	s_cbranch_scc1 .Lp1vg_w11_b2
	s_waitcnt vmcnt(8)
	s_branch .Lp1vg_wd_b2

.Lp1vg_wd_b2:
	s_waitcnt lgkmcnt(0)
	s_barrier
	s_setprio 1
	s_waitcnt lgkmcnt(0)
	v_mfma_f32_16x16x32_bf16 v[74:77], v[158:161], v[174:177], v[74:77]
	v_mfma_f32_16x16x32_bf16 v[70:73], v[166:169], v[174:177], v[70:73]
	v_mfma_f32_16x16x32_bf16 v[58:61], v[158:161], v[182:185], v[58:61]
	v_mfma_f32_16x16x32_bf16 v[54:57], v[166:169], v[182:185], v[54:57]
	v_mfma_f32_16x16x32_bf16 v[42:45], v[158:161], v[190:193], v[42:45]
	v_mfma_f32_16x16x32_bf16 v[38:41], v[166:169], v[190:193], v[38:41]
	v_mfma_f32_16x16x32_bf16 v[26:29], v[158:161], v[198:201], v[26:29]
	v_mfma_f32_16x16x32_bf16 v[22:25], v[166:169], v[198:201], v[22:25]
	v_mfma_f32_16x16x32_bf16 v[74:77], v[162:165], v[178:181], v[74:77]
	v_mfma_f32_16x16x32_bf16 v[70:73], v[170:173], v[178:181], v[70:73]
	v_mfma_f32_16x16x32_bf16 v[58:61], v[162:165], v[186:189], v[58:61]
	v_mfma_f32_16x16x32_bf16 v[54:57], v[170:173], v[186:189], v[54:57]
	v_mfma_f32_16x16x32_bf16 v[42:45], v[162:165], v[194:197], v[42:45]
	v_mfma_f32_16x16x32_bf16 v[38:41], v[170:173], v[194:197], v[38:41]
	v_mfma_f32_16x16x32_bf16 v[26:29], v[162:165], v[202:205], v[26:29]
	v_mfma_f32_16x16x32_bf16 v[22:25], v[170:173], v[202:205], v[22:25]
	s_setprio 0
	s_setprio 1
	v_mfma_f32_16x16x32_bf16 v[66:69], v[142:145], v[174:177], v[66:69]
	v_mfma_f32_16x16x32_bf16 v[62:65], v[150:153], v[174:177], v[62:65]
	v_mfma_f32_16x16x32_bf16 v[50:53], v[142:145], v[182:185], v[50:53]
	v_mfma_f32_16x16x32_bf16 v[46:49], v[150:153], v[182:185], v[46:49]
	v_mfma_f32_16x16x32_bf16 v[34:37], v[142:145], v[190:193], v[34:37]
	v_mfma_f32_16x16x32_bf16 v[30:33], v[150:153], v[190:193], v[30:33]
	v_mfma_f32_16x16x32_bf16 v[18:21], v[142:145], v[198:201], v[18:21]
	v_mfma_f32_16x16x32_bf16 v[14:17], v[150:153], v[198:201], v[14:17]
	v_mfma_f32_16x16x32_bf16 v[66:69], v[146:149], v[178:181], v[66:69]
	v_mfma_f32_16x16x32_bf16 v[62:65], v[154:157], v[178:181], v[62:65]
	v_mfma_f32_16x16x32_bf16 v[50:53], v[146:149], v[186:189], v[50:53]
	v_mfma_f32_16x16x32_bf16 v[46:49], v[154:157], v[186:189], v[46:49]
	v_mfma_f32_16x16x32_bf16 v[34:37], v[146:149], v[194:197], v[34:37]
	v_mfma_f32_16x16x32_bf16 v[30:33], v[154:157], v[194:197], v[30:33]
	v_mfma_f32_16x16x32_bf16 v[18:21], v[146:149], v[202:205], v[18:21]
	v_mfma_f32_16x16x32_bf16 v[14:17], v[154:157], v[202:205], v[14:17]
	s_setprio 0
	s_barrier
	s_add_i32 s81, s81, 2
	s_add_u32 s54, s54, 0x100
	s_addc_u32 s55, s55, 0
	s_add_u32 s79, s79, 0x100
	s_addc_u32 s80, s80, 0
	s_cmp_gt_u32 s81, 29
	s_cbranch_scc1 .LBB0_180
.LBB0_168:
	ds_read_b128 v[158:161], v232
	ds_read_b128 v[162:165], v232 offset:1024
	ds_read_b128 v[166:169], v232 offset:2048
	ds_read_b128 v[170:173], v232 offset:3072
	ds_read_b128 v[142:145], v233
	ds_read_b128 v[146:149], v233 offset:1024
	ds_read_b128 v[150:153], v233 offset:2048
	ds_read_b128 v[154:157], v233 offset:3072
	v_lshl_add_u64 v[4:5], s[54:55], 0, v[218:219]
	s_add_i32 m0, s41, 0xc000
	ds_read_b128 v[198:201], v234
	ds_read_b128 v[202:205], v234 offset:1024
	ds_read_b128 v[190:193], v234 offset:2048
	ds_read_b128 v[194:197], v234 offset:3072
	ds_read_b128 v[182:185], v234 offset:4096
	ds_read_b128 v[186:189], v234 offset:5120
	ds_read_b128 v[174:177], v234 offset:6144
	ds_read_b128 v[178:181], v234 offset:7168
	global_load_lds_dwordx4 v[4:5], off
	v_lshl_add_u64 v[4:5], s[54:55], 0, v[220:221]
	s_add_i32 m0, s41, 0xe000
	s_nop 0
	global_load_lds_dwordx4 v[4:5], off
	s_cmp_eq_u32 s100, 3
	s_cbranch_scc1 .Lp1vg_w11_a1
	s_waitcnt vmcnt(8)
	s_branch .Lp1vg_wd_a1

; #define PG8_LAS __attribute__((address_space(3)))
;     __device__ __forceinline__ void issue(PG8_LAS unsigned char* lds0, int j, int tid, int wid) const {
;         const float* s0; unsigned char* d; addr(j, tid, s0, d);
;         __builtin_amdgcn_global_load_lds((const unsigned*)s0, (PG8_LAS unsigned*)(lds0 + stage + wid * 1024), 16, 0, 2);
;         __builtin_amdgcn_global_load_lds((const unsigned*)(s0 + ntot), (PG8_LAS unsigned*)(lds0 + stage + 8192 + wid * 1024), 16, 0, 2);
;     }
;     __device__ __forceinline__ void read(v4i_t& t0, v4i_t& t1, int tid, unsigned ldsb) const {
;         asm volatile("ds_read_b128 %0, %1" : "=&v"(t0) : "v"(ldsb + stage + 16u * (unsigned)tid) : "memory");
;         asm volatile("ds_read_b128 %0, %1" : "=&v"(t1) : "v"(ldsb + stage + 8192u + 16u * (unsigned)tid) : "memory");
;     }
;     __device__ __forceinline__ void finish(v4i_t& t0, v4i_t& t1, int j, int tid) const {
;         asm volatile("" : "+v"(t0), "+v"(t1));
;         const float* s0; unsigned char* d; addr(j, tid, s0, d);
;         const f32x4 r0 = __builtin_bit_cast(f32x4, t0) * 64.f, r1 = __builtin_bit_cast(f32x4, t1) * 64.f;
;         int w0 = 0, w1 = 0; w0 = __builtin_amdgcn_cvt_pk_fp8_f32(r0[0], r1[0], w0, false); w0 = __builtin_amdgcn_cvt_pk_fp8_f32(r0[1], r1[1], w0, true);
;         w1 = __builtin_amdgcn_cvt_pk_fp8_f32(r0[2], r1[2], w1, false); w1 = __builtin_amdgcn_cvt_pk_fp8_f32(r0[3], r1[3], w1, true);
;         typedef int v2is __attribute__((ext_vector_type(2))); __builtin_nontemporal_store((v2is){w0, w1}, (v2is*)d);
.Lp1vg_wd_a1:
	s_waitcnt lgkmcnt(0)
	s_mov_b32 s100, 0
	s_cmp_lt_i32 s98, 0
	s_cbranch_scc1 .Lp1vg_nf_a
	s_add_i32 s4, s98, s68
	s_lshr_b32 s2, s4, 31
	s_add_i32 s2, s4, s2
	s_ashr_i32 s5, s2, 1
	s_ashr_i32 s2, s2, 11
	s_and_b32 s3, s5, 0x3ff
	s_ashr_i32 s56, s2, 31
	s_lshl_b32 s2, s2, 10
	v_pk_mul_f32 v[6:7], v[6:7], s[40:41] op_sel_hi:[1,0]
	v_pk_mul_f32 v[8:9], v[8:9], s[40:41] op_sel_hi:[1,0]
	v_pk_mul_f32 v[10:11], v[10:11], s[40:41] op_sel_hi:[1,0]
	v_pk_mul_f32 v[12:13], v[12:13], s[40:41] op_sel_hi:[1,0]
	s_or_b32 s2, s2, s3
	v_cvt_pk_fp8_f32 v6, v6, v10
	s_mul_hi_u32 s3, s2, 0x2100
	s_mulk_i32 s56, 0x2100
	v_cvt_pk_fp8_f32 v6, v7, v11 op_sel:[0,0,1]
	s_add_i32 s3, s3, s56
	s_mulk_i32 s2, 0x2100
	v_cvt_pk_fp8_f32 v7, v8, v12
	v_readlane_b32 s101, v251, 49
	s_add_u32 s2, s101, s2
	v_readlane_b32 s101, v251, 31
	s_addc_u32 s3, s101, s3
	v_cvt_pk_fp8_f32 v7, v9, v13 op_sel:[0,0,1]
	v_lshl_or_b32 v226, s4, 11, v208
	s_lshl_b32 s56, s5, 12
	v_subrev_u32_e32 v4, s56, v226
	v_ashrrev_i32_e32 v5, 31, v4
	v_lshl_add_u64 v[4:5], v[4:5], 1, s[2:3]
	global_store_dwordx2 v[4:5], v[6:7], off nt
	s_mov_b32 s100, 1
.Lp1vg_nf_a:
	s_mov_b32 s98, -1
	s_cmpk_gt_i32 s77, 0x5f
	s_cbranch_scc1 .Lp1vg_ni_a
	s_add_i32 s4, s77, s68
	s_lshr_b32 s2, s4, 31
	s_add_i32 s2, s4, s2
	s_ashr_i32 s5, s2, 1
	s_ashr_i32 s2, s2, 11
	s_ashr_i32 s3, s2, 31
	s_lshl_b64 s[2:3], s[2:3], 25
	v_readlane_b32 s82, v251, 36
	v_readlane_b32 s83, v251, 37
	s_add_u32 s2, s82, s2
	s_addc_u32 s3, s83, s3
	s_lshl_b32 s82, s5, 15
	s_and_b32 s82, s82, 0x1ff8000
	s_add_u32 s82, s2, s82
	s_addc_u32 s83, s3, 0
	s_lshl_b32 s2, s5, 12
	s_lshl_b32 s3, s4, 11
	s_sub_i32 s2, s3, s2
	s_ashr_i32 s3, s2, 31
	s_lshl_b64 s[2:3], s[2:3], 2
	s_add_u32 s2, s82, s2
	s_addc_u32 s3, s83, s3
	v_lshlrev_b32_e32 v2, 2, v208
	v_lshl_add_u64 v[4:5], s[2:3], 0, v[2:3]
	v_lshl_add_u64 v[4:5], v[4:5], 0, s[42:43]
	global_load_dwordx4 v[6:9], v2, s[2:3] nt
	global_load_dwordx4 v[10:13], v[4:5], off nt
	s_mov_b32 s98, s77
	s_add_i32 s77, s77, 1
	s_add_i32 s100, s100, 2
.Lp1vg_ni_a:
.LBB0_174:
	s_add_u32 s4, s54, 0xfff80080
	s_addc_u32 s5, s55, -1
	s_cmp_eq_u32 s81, 28
	s_cselect_b32 s5, s7, s5
	s_cselect_b32 s4, s33, s4
	s_cselect_b32 s57, s45, s80
	s_cselect_b32 s56, s47, s79
	s_barrier
	s_setprio 1
	s_waitcnt lgkmcnt(0)
	v_mfma_f32_16x16x32_bf16 v[138:141], v[158:161], v[198:201], v[138:141]
	v_mfma_f32_16x16x32_bf16 v[134:137], v[166:169], v[198:201], v[134:137]
	v_mfma_f32_16x16x32_bf16 v[122:125], v[158:161], v[190:193], v[122:125]
	v_mfma_f32_16x16x32_bf16 v[118:121], v[166:169], v[190:193], v[118:121]
	v_mfma_f32_16x16x32_bf16 v[106:109], v[158:161], v[182:185], v[106:109]
	v_mfma_f32_16x16x32_bf16 v[102:105], v[166:169], v[182:185], v[102:105]
	v_mfma_f32_16x16x32_bf16 v[90:93], v[158:161], v[174:177], v[90:93]
	v_mfma_f32_16x16x32_bf16 v[86:89], v[166:169], v[174:177], v[86:89]
	v_mfma_f32_16x16x32_bf16 v[138:141], v[162:165], v[202:205], v[138:141]
	v_mfma_f32_16x16x32_bf16 v[134:137], v[170:173], v[202:205], v[134:137]
	v_mfma_f32_16x16x32_bf16 v[122:125], v[162:165], v[194:197], v[122:125]
	v_mfma_f32_16x16x32_bf16 v[118:121], v[170:173], v[194:197], v[118:121]
	v_mfma_f32_16x16x32_bf16 v[106:109], v[162:165], v[186:189], v[106:109]
	v_mfma_f32_16x16x32_bf16 v[102:105], v[170:173], v[186:189], v[102:105]
	v_mfma_f32_16x16x32_bf16 v[90:93], v[162:165], v[178:181], v[90:93]
	v_mfma_f32_16x16x32_bf16 v[86:89], v[170:173], v[178:181], v[86:89]
	s_setprio 0
	s_setprio 1
	v_mfma_f32_16x16x32_bf16 v[130:133], v[142:145], v[198:201], v[130:133]
	v_mfma_f32_16x16x32_bf16 v[126:129], v[150:153], v[198:201], v[126:129]
	v_mfma_f32_16x16x32_bf16 v[114:117], v[142:145], v[190:193], v[114:117]
	v_mfma_f32_16x16x32_bf16 v[110:113], v[150:153], v[190:193], v[110:113]
	v_mfma_f32_16x16x32_bf16 v[98:101], v[142:145], v[182:185], v[98:101]
	v_mfma_f32_16x16x32_bf16 v[94:97], v[150:153], v[182:185], v[94:97]
	v_mfma_f32_16x16x32_bf16 v[82:85], v[142:145], v[174:177], v[82:85]
	v_mfma_f32_16x16x32_bf16 v[78:81], v[150:153], v[174:177], v[78:81]
	v_mfma_f32_16x16x32_bf16 v[130:133], v[146:149], v[202:205], v[130:133]
	v_mfma_f32_16x16x32_bf16 v[126:129], v[154:157], v[202:205], v[126:129]
	v_mfma_f32_16x16x32_bf16 v[114:117], v[146:149], v[194:197], v[114:117]
	v_mfma_f32_16x16x32_bf16 v[110:113], v[154:157], v[194:197], v[110:113]
	v_mfma_f32_16x16x32_bf16 v[98:101], v[146:149], v[186:189], v[98:101]
	v_mfma_f32_16x16x32_bf16 v[94:97], v[154:157], v[186:189], v[94:97]
	v_mfma_f32_16x16x32_bf16 v[82:85], v[146:149], v[178:181], v[82:85]
	v_mfma_f32_16x16x32_bf16 v[78:81], v[154:157], v[178:181], v[78:81]
	s_setprio 0
	s_barrier
	s_mov_b32 m0, s53
	v_lshl_add_u64 v[4:5], s[56:57], 0, v[212:213]
	s_add_u32 s82, s56, 0x80000
	ds_read_b128 v[174:177], v234 offset:16384
	ds_read_b128 v[178:181], v234 offset:17408
	ds_read_b128 v[182:185], v234 offset:18432
	ds_read_b128 v[186:189], v234 offset:19456
	ds_read_b128 v[190:193], v234 offset:20480
	ds_read_b128 v[194:197], v234 offset:21504
	ds_read_b128 v[198:201], v234 offset:22528
	ds_read_b128 v[202:205], v234 offset:23552
	global_load_lds_dwordx4 v[4:5], off
	v_lshl_add_u64 v[226:227], s[56:57], 0, v[216:217]
	s_mov_b32 m0, s60
	s_addc_u32 s83, s57, 0
	global_load_lds_dwordx4 v[226:227], off
	v_lshl_add_u64 v[228:229], s[82:83], 0, v[212:213]
	s_mov_b32 m0, s61
	v_lshl_add_u64 v[230:231], s[4:5], 0, v[214:215]
	global_load_lds_dwordx4 v[228:229], off
	v_lshl_add_u64 v[228:229], s[82:83], 0, v[216:217]
	s_mov_b32 m0, s64
	s_nop 0
	global_load_lds_dwordx4 v[228:229], off
	v_lshl_add_u64 v[228:229], s[4:5], 0, v[210:211]
	s_mov_b32 m0, s41
	s_nop 0
	global_load_lds_dwordx4 v[228:229], off
	s_mov_b32 m0, s65
	s_nop 0
	global_load_lds_dwordx4 v[230:231], off
	s_cmp_eq_u32 s100, 3
	s_cbranch_scc1 .Lp1vg_w11_a2
	s_waitcnt vmcnt(8)
	s_branch .Lp1vg_wd_a2

.Lp1vg_wd_a2:
	s_waitcnt lgkmcnt(0)
	s_barrier
	s_setprio 1
	s_waitcnt lgkmcnt(0)
	v_mfma_f32_16x16x32_bf16 v[74:77], v[158:161], v[174:177], v[74:77]
	v_mfma_f32_16x16x32_bf16 v[70:73], v[166:169], v[174:177], v[70:73]
	v_mfma_f32_16x16x32_bf16 v[58:61], v[158:161], v[182:185], v[58:61]
	v_mfma_f32_16x16x32_bf16 v[54:57], v[166:169], v[182:185], v[54:57]
	v_mfma_f32_16x16x32_bf16 v[42:45], v[158:161], v[190:193], v[42:45]
	v_mfma_f32_16x16x32_bf16 v[38:41], v[166:169], v[190:193], v[38:41]
	v_mfma_f32_16x16x32_bf16 v[26:29], v[158:161], v[198:201], v[26:29]
	v_mfma_f32_16x16x32_bf16 v[22:25], v[166:169], v[198:201], v[22:25]
	v_mfma_f32_16x16x32_bf16 v[74:77], v[162:165], v[178:181], v[74:77]
	v_mfma_f32_16x16x32_bf16 v[70:73], v[170:173], v[178:181], v[70:73]
	v_mfma_f32_16x16x32_bf16 v[58:61], v[162:165], v[186:189], v[58:61]
	v_mfma_f32_16x16x32_bf16 v[54:57], v[170:173], v[186:189], v[54:57]
	v_mfma_f32_16x16x32_bf16 v[42:45], v[162:165], v[194:197], v[42:45]
	v_mfma_f32_16x16x32_bf16 v[38:41], v[170:173], v[194:197], v[38:41]
	v_mfma_f32_16x16x32_bf16 v[26:29], v[162:165], v[202:205], v[26:29]
	v_mfma_f32_16x16x32_bf16 v[22:25], v[170:173], v[202:205], v[22:25]
	s_setprio 0
	s_setprio 1
	v_mfma_f32_16x16x32_bf16 v[66:69], v[142:145], v[174:177], v[66:69]
	v_mfma_f32_16x16x32_bf16 v[62:65], v[150:153], v[174:177], v[62:65]
	v_mfma_f32_16x16x32_bf16 v[50:53], v[142:145], v[182:185], v[50:53]
	v_mfma_f32_16x16x32_bf16 v[46:49], v[150:153], v[182:185], v[46:49]
	v_mfma_f32_16x16x32_bf16 v[34:37], v[142:145], v[190:193], v[34:37]
	v_mfma_f32_16x16x32_bf16 v[30:33], v[150:153], v[190:193], v[30:33]
	v_mfma_f32_16x16x32_bf16 v[18:21], v[142:145], v[198:201], v[18:21]
	v_mfma_f32_16x16x32_bf16 v[14:17], v[150:153], v[198:201], v[14:17]
	v_mfma_f32_16x16x32_bf16 v[66:69], v[146:149], v[178:181], v[66:69]
	v_mfma_f32_16x16x32_bf16 v[62:65], v[154:157], v[178:181], v[62:65]
	v_mfma_f32_16x16x32_bf16 v[50:53], v[146:149], v[186:189], v[50:53]
	v_mfma_f32_16x16x32_bf16 v[46:49], v[154:157], v[186:189], v[46:49]
	v_mfma_f32_16x16x32_bf16 v[34:37], v[146:149], v[194:197], v[34:37]
	v_mfma_f32_16x16x32_bf16 v[30:33], v[154:157], v[194:197], v[30:33]
	v_mfma_f32_16x16x32_bf16 v[18:21], v[146:149], v[202:205], v[18:21]
	v_mfma_f32_16x16x32_bf16 v[14:17], v[154:157], v[202:205], v[14:17]
	s_setprio 0
	s_barrier
	v_add_u32_e32 v2, 0x18000, v209
	ds_read_b128 v[158:161], v2
	ds_read_b128 v[162:165], v2 offset:1024
	ds_read_b128 v[166:169], v2 offset:2048
	ds_read_b128 v[170:173], v2 offset:3072
	v_add_u32_e32 v2, 0x1c000, v209
	ds_read_b128 v[142:145], v2
	ds_read_b128 v[146:149], v2 offset:1024
	ds_read_b128 v[150:153], v2 offset:2048
	ds_read_b128 v[154:157], v2 offset:3072
	s_add_u32 s4, s4, 0x80000
	s_addc_u32 s5, s5, 0
	s_mov_b32 m0, s66
	v_lshl_add_u64 v[238:239], s[4:5], 0, v[210:211]
	ds_read_b128 v[198:201], v234 offset:32768
	ds_read_b128 v[202:205], v234 offset:33792
	ds_read_b128 v[190:193], v234 offset:34816
	ds_read_b128 v[194:197], v234 offset:35840
	ds_read_b128 v[182:185], v234 offset:36864
	ds_read_b128 v[186:189], v234 offset:37888
	ds_read_b128 v[174:177], v234 offset:38912
	ds_read_b128 v[178:181], v234 offset:39936
	global_load_lds_dwordx4 v[238:239], off
	v_lshl_add_u64 v[238:239], s[4:5], 0, v[214:215]
	s_mov_b32 m0, s67
	s_nop 0
	global_load_lds_dwordx4 v[238:239], off
	s_cmp_eq_u32 s100, 3
	s_cbranch_scc1 .Lp1vg_w11_b1
	s_waitcnt vmcnt(8)
	s_branch .Lp1vg_wd_b1

; #define PG8_LAS __attribute__((address_space(3)))
;     __device__ __forceinline__ void issue(PG8_LAS unsigned char* lds0, int j, int tid, int wid) const {
;         const float* s0; unsigned char* d; addr(j, tid, s0, d);
;         __builtin_amdgcn_global_load_lds((const unsigned*)s0, (PG8_LAS unsigned*)(lds0 + stage + wid * 1024), 16, 0, 2);
;         __builtin_amdgcn_global_load_lds((const unsigned*)(s0 + ntot), (PG8_LAS unsigned*)(lds0 + stage + 8192 + wid * 1024), 16, 0, 2);
;     }
;     __device__ __forceinline__ void read(v4i_t& t0, v4i_t& t1, int tid, unsigned ldsb) const {
;         asm volatile("ds_read_b128 %0, %1" : "=&v"(t0) : "v"(ldsb + stage + 16u * (unsigned)tid) : "memory");
;         asm volatile("ds_read_b128 %0, %1" : "=&v"(t1) : "v"(ldsb + stage + 8192u + 16u * (unsigned)tid) : "memory");
;     }
;     __device__ __forceinline__ void finish(v4i_t& t0, v4i_t& t1, int j, int tid) const {
;         asm volatile("" : "+v"(t0), "+v"(t1));
;         const float* s0; unsigned char* d; addr(j, tid, s0, d);
;         const f32x4 r0 = __builtin_bit_cast(f32x4, t0) * 64.f, r1 = __builtin_bit_cast(f32x4, t1) * 64.f;
;         int w0 = 0, w1 = 0; w0 = __builtin_amdgcn_cvt_pk_fp8_f32(r0[0], r1[0], w0, false); w0 = __builtin_amdgcn_cvt_pk_fp8_f32(r0[1], r1[1], w0, true);
;         w1 = __builtin_amdgcn_cvt_pk_fp8_f32(r0[2], r1[2], w1, false); w1 = __builtin_amdgcn_cvt_pk_fp8_f32(r0[3], r1[3], w1, true);
;         typedef int v2is __attribute__((ext_vector_type(2))); __builtin_nontemporal_store((v2is){w0, w1}, (v2is*)d);
.Lp1vg_wd_b1:
	s_waitcnt lgkmcnt(0)
	s_mov_b32 s100, 0
	s_cmp_lt_i32 s99, 0
	s_cbranch_scc1 .Lp1vg_nf_b
	s_add_i32 s4, s99, s68
	s_lshr_b32 s2, s4, 31
	s_add_i32 s2, s4, s2
	s_ashr_i32 s5, s2, 1
	s_ashr_i32 s2, s2, 11
	s_and_b32 s3, s5, 0x3ff
	s_ashr_i32 s82, s2, 31
	s_lshl_b32 s2, s2, 10
	v_pk_mul_f32 v[240:241], v[240:241], s[40:41] op_sel_hi:[1,0]
	v_pk_mul_f32 v[242:243], v[242:243], s[40:41] op_sel_hi:[1,0]
	v_pk_mul_f32 v[244:245], v[244:245], s[40:41] op_sel_hi:[1,0]
	v_pk_mul_f32 v[246:247], v[246:247], s[40:41] op_sel_hi:[1,0]
	s_or_b32 s2, s2, s3
	v_cvt_pk_fp8_f32 v240, v240, v244
	s_mul_hi_u32 s3, s2, 0x2100
	s_mulk_i32 s82, 0x2100
	v_cvt_pk_fp8_f32 v240, v241, v245 op_sel:[0,0,1]
	s_add_i32 s3, s3, s82
	s_mulk_i32 s2, 0x2100
	v_cvt_pk_fp8_f32 v241, v242, v246
	v_readlane_b32 s101, v251, 49
	s_add_u32 s2, s101, s2
	v_readlane_b32 s101, v251, 31
	s_addc_u32 s3, s101, s3
	v_cvt_pk_fp8_f32 v241, v243, v247 op_sel:[0,0,1]
	v_lshl_or_b32 v248, s4, 11, v208
	s_lshl_b32 s82, s5, 12
	v_subrev_u32_e32 v238, s82, v248
	v_ashrrev_i32_e32 v239, 31, v238
	v_lshl_add_u64 v[238:239], v[238:239], 1, s[2:3]
	global_store_dwordx2 v[238:239], v[240:241], off nt
	s_mov_b32 s100, 1
.Lp1vg_nf_b:
	s_mov_b32 s99, -1
	s_cmpk_gt_i32 s77, 0x5f
	s_cbranch_scc1 .Lp1vg_ni_b
	s_add_i32 s4, s77, s68
	s_lshr_b32 s2, s4, 31
	s_add_i32 s2, s4, s2
	s_ashr_i32 s5, s2, 1
	s_ashr_i32 s2, s2, 11
	s_ashr_i32 s3, s2, 31
	s_lshl_b64 s[2:3], s[2:3], 25
	v_readlane_b32 s84, v251, 36
	v_readlane_b32 s85, v251, 37
	s_add_u32 s2, s84, s2
	s_addc_u32 s3, s85, s3
	s_lshl_b32 s84, s5, 15
	s_and_b32 s84, s84, 0x1ff8000
	s_add_u32 s84, s2, s84
	s_addc_u32 s85, s3, 0
	s_lshl_b32 s2, s5, 12
	s_lshl_b32 s3, s4, 11
	s_sub_i32 s2, s3, s2
	s_ashr_i32 s3, s2, 31
	s_lshl_b64 s[2:3], s[2:3], 2
	s_add_u32 s2, s84, s2
	s_addc_u32 s3, s85, s3
	v_lshlrev_b32_e32 v2, 2, v208
	v_lshl_add_u64 v[238:239], s[2:3], 0, v[2:3]
	v_lshl_add_u64 v[238:239], v[238:239], 0, s[42:43]
	global_load_dwordx4 v[240:243], v2, s[2:3] nt
	global_load_dwordx4 v[244:247], v[238:239], off nt
	s_mov_b32 s99, s77
	s_add_i32 s77, s77, 1
	s_add_i32 s100, s100, 2
.Lp1vg_ni_b:
	s_branch .LBB0_167

;     __device__ __forceinline__ void finish(v4i_t& t0, v4i_t& t1, int j, int tid) const {
;         asm volatile("" : "+v"(t0), "+v"(t1));
;         const float* s0; unsigned char* d; addr(j, tid, s0, d);
;         const f32x4 r0 = __builtin_bit_cast(f32x4, t0) * 64.f, r1 = __builtin_bit_cast(f32x4, t1) * 64.f;
;         int w0 = 0, w1 = 0; w0 = __builtin_amdgcn_cvt_pk_fp8_f32(r0[0], r1[0], w0, false); w0 = __builtin_amdgcn_cvt_pk_fp8_f32(r0[1], r1[1], w0, true);
;         w1 = __builtin_amdgcn_cvt_pk_fp8_f32(r0[2], r1[2], w1, false); w1 = __builtin_amdgcn_cvt_pk_fp8_f32(r0[3], r1[3], w1, true);
;         typedef int v2is __attribute__((ext_vector_type(2))); __builtin_nontemporal_store((v2is){w0, w1}, (v2is*)d);
;     }
.LBB0_237:
	s_waitcnt vmcnt(0)
	s_mov_b32 s90, s86
	s_barrier
	s_mov_b32 s4, 0x42800000
	s_cmp_lt_i32 s98, 0
	s_cbranch_scc1 .Lp1vg_dx
	s_add_i32 s6, s98, s68
	s_lshr_b32 s2, s6, 31
	s_add_i32 s2, s6, s2
	s_ashr_i32 s101, s2, 1
	s_ashr_i32 s2, s2, 11
	s_and_b32 s3, s101, 0x3ff
	s_ashr_i32 s7, s2, 31
	s_lshl_b32 s2, s2, 10
	v_pk_mul_f32 v[6:7], v[6:7], s[4:5] op_sel_hi:[1,0]
	v_pk_mul_f32 v[8:9], v[8:9], s[4:5] op_sel_hi:[1,0]
	v_pk_mul_f32 v[10:11], v[10:11], s[4:5] op_sel_hi:[1,0]
	v_pk_mul_f32 v[12:13], v[12:13], s[4:5] op_sel_hi:[1,0]
	s_or_b32 s2, s2, s3
	v_cvt_pk_fp8_f32 v6, v6, v10
	s_mul_hi_u32 s3, s2, 0x2100
	s_mulk_i32 s7, 0x2100
	v_cvt_pk_fp8_f32 v6, v7, v11 op_sel:[0,0,1]
	s_add_i32 s3, s3, s7
	s_mulk_i32 s2, 0x2100
	v_cvt_pk_fp8_f32 v7, v8, v12
	v_readlane_b32 s100, v251, 49
	s_add_u32 s2, s100, s2
	v_readlane_b32 s100, v251, 31
	s_addc_u32 s3, s100, s3
	v_cvt_pk_fp8_f32 v7, v9, v13 op_sel:[0,0,1]
	v_lshl_or_b32 v14, s6, 11, v208
	s_lshl_b32 s7, s101, 12
	v_subrev_u32_e32 v2, s7, v14
	v_ashrrev_i32_e32 v3, 31, v2
	v_lshl_add_u64 v[2:3], v[2:3], 1, s[2:3]
	global_store_dwordx2 v[2:3], v[6:7], off nt
.Lp1vg_dx:
	s_cmp_lt_i32 s99, 0
	s_cbranch_scc1 .Lp1vg_dy
	s_add_i32 s6, s99, s68
	s_lshr_b32 s2, s6, 31
	s_add_i32 s2, s6, s2
	s_ashr_i32 s101, s2, 1
	s_ashr_i32 s2, s2, 11
	s_and_b32 s3, s101, 0x3ff
	s_ashr_i32 s7, s2, 31
	s_lshl_b32 s2, s2, 10
	v_pk_mul_f32 v[240:241], v[240:241], s[4:5] op_sel_hi:[1,0]
	v_pk_mul_f32 v[242:243], v[242:243], s[4:5] op_sel_hi:[1,0]
	v_pk_mul_f32 v[244:245], v[244:245], s[4:5] op_sel_hi:[1,0]
	v_pk_mul_f32 v[246:247], v[246:247], s[4:5] op_sel_hi:[1,0]
	s_or_b32 s2, s2, s3
	v_cvt_pk_fp8_f32 v240, v240, v244
	s_mul_hi_u32 s3, s2, 0x2100
	s_mulk_i32 s7, 0x2100
	v_cvt_pk_fp8_f32 v240, v241, v245 op_sel:[0,0,1]
	s_add_i32 s3, s3, s7
	s_mulk_i32 s2, 0x2100
	v_cvt_pk_fp8_f32 v241, v242, v246
	v_readlane_b32 s100, v251, 49
	s_add_u32 s2, s100, s2
	v_readlane_b32 s100, v251, 31
	s_addc_u32 s3, s100, s3
	v_cvt_pk_fp8_f32 v241, v243, v247 op_sel:[0,0,1]
	v_lshl_or_b32 v14, s6, 11, v208
	s_lshl_b32 s7, s101, 12
	v_subrev_u32_e32 v2, s7, v14
	v_ashrrev_i32_e32 v3, 31, v2
	v_lshl_add_u64 v[2:3], v[2:3], 1, s[2:3]
	global_store_dwordx2 v[2:3], v[240:241], off nt
.Lp1vg_dy:
.LBB0_239:
	s_barrier
	s_mov_b64 s[2:3], exec
	v_readlane_b32 s4, v251, 23
	v_readlane_b32 s5, v251, 24
	v_readlane_b32 s20, v251, 25
	s_and_b64 s[4:5], s[2:3], s[4:5]
	v_readlane_b32 s21, v251, 26
	v_readlane_b32 s22, v251, 27
	v_readlane_b32 s23, v251, 28
	s_mov_b64 exec, s[4:5]
	s_cbranch_execz .LBB0_242
	s_mov_b64 s[4:5], exec
	v_mbcnt_lo_u32_b32 v1, s4, 0
	v_mbcnt_hi_u32_b32 v1, s5, v1
	v_cmp_eq_u32_e32 vcc, 0, v1
	s_and_b64 s[6:7], exec, vcc
	s_mov_b64 exec, s[6:7]
	s_cbranch_execz .LBB0_242
	s_bcnt1_i32_b64 s4, s[4:5]
	v_mov_b32_e32 v1, 0x14000
	v_mov_b32_e32 v2, s4
	global_atomic_add v1, v2, s[20:21]
